# grid barrier: acquire invalidate issued right behind the arrival atomic (overlaps the arrival round trip and the wait)
# speedup vs baseline: 1.0246x; 1.0035x over previous
.LBB0_193:
	v_readlane_b32 s4, v251, 48
	s_lshl_b32 s4, s4, 2
	s_add_u32 s25, s2, s4
	s_addc_u32 s24, s3, 0
	v_mov_b32_e32 v1, s25
	v_add_co_u32_e32 v8, vcc, 0x1000, v1
	v_mov_b32_e32 v1, s24
	s_nop 0
	v_addc_co_u32_e32 v9, vcc, 0, v1, vcc
	flat_atomic_add v1, v[8:9], v211 offset:1024 sc0
	buffer_inv sc1
	v_cvt_f32_u32_e32 v3, v6
	v_sub_u32_e32 v5, 0, v6
	v_rcp_iflag_f32_e32 v3, v3
	s_nop 0
	v_mul_f32_e32 v3, 0x4f7ffffe, v3
	v_cvt_u32_f32_e32 v3, v3
	v_mul_lo_u32 v5, v5, v3
	v_mul_hi_u32 v5, v3, v5
	v_add_u32_e32 v3, v3, v5
	s_waitcnt vmcnt(0) lgkmcnt(0)
	v_mul_hi_u32 v3, v1, v3
	v_mul_lo_u32 v7, v3, v6
	v_add_u32_e32 v5, 1, v1
	v_sub_u32_e32 v1, v1, v7
	v_add_u32_e32 v8, 1, v3
	v_cmp_ge_u32_e32 vcc, v1, v6
	v_sub_u32_e32 v7, v1, v6
	s_nop 0
	v_cndmask_b32_e32 v3, v3, v8, vcc
	v_cndmask_b32_e32 v1, v1, v7, vcc
	v_add_u32_e32 v7, 1, v3
	v_cmp_ge_u32_e32 vcc, v1, v6
	s_nop 1
	v_cndmask_b32_e32 v1, v3, v7, vcc
	v_mad_u64_u32 v[6:7], s[4:5], v6, v1, v[6:7]
	v_cmp_ne_u32_e32 vcc, v5, v6
	s_and_saveexec_b64 s[4:5], vcc
	s_xor_b64 s[4:5], exec, s[4:5]
	s_cbranch_execz .LBB0_206
	v_mad_u32_u24 v255, v4, v1, 1
	v_mov_b32_e32 v3, s25
	v_add_co_u32_e32 v4, vcc, 0x2000, v3
	v_mov_b32_e32 v3, s24
	s_nop 0
	v_addc_co_u32_e32 v5, vcc, 0, v3, vcc
	flat_load_dword v3, v[4:5] offset:1024 sc1
	s_add_u32 s8, s25, 0x2400
	s_addc_u32 s9, s24, 0
	s_waitcnt vmcnt(0) lgkmcnt(0)
	v_cmp_lt_u32_e32 vcc, v3, v255
	s_and_saveexec_b64 s[6:7], vcc
	s_cbranch_execz .LBB0_205
	s_mov_b32 s26, 1
	s_mov_b64 s[10:11], 0
	s_branch .LBB0_197

.LBB0_360:
	v_readlane_b32 s4, v251, 48
	s_lshl_b32 s4, s4, 2
	s_add_u32 s25, s2, s4
	s_addc_u32 s24, s3, 0
	v_mov_b32_e32 v1, s25
	v_add_co_u32_e32 v8, vcc, 0x1000, v1
	v_mov_b32_e32 v1, s24
	s_nop 0
	v_addc_co_u32_e32 v9, vcc, 0, v1, vcc
	flat_atomic_add v3, v[8:9], v211 offset:1024 sc0
	buffer_inv sc1
	v_cvt_f32_u32_e32 v1, v6
	v_sub_u32_e32 v5, 0, v6
	v_rcp_iflag_f32_e32 v1, v1
	s_nop 0
	v_mul_f32_e32 v1, 0x4f7ffffe, v1
	v_cvt_u32_f32_e32 v1, v1
	v_mul_lo_u32 v5, v5, v1
	v_mul_hi_u32 v5, v1, v5
	v_add_u32_e32 v1, v1, v5
	s_waitcnt vmcnt(0) lgkmcnt(0)
	v_mul_hi_u32 v1, v3, v1
	v_mul_lo_u32 v5, v1, v6
	v_sub_u32_e32 v5, v3, v5
	v_cmp_ge_u32_e32 vcc, v5, v6
	v_add_u32_e32 v7, 1, v1
	v_add_u32_e32 v3, 1, v3
	v_cndmask_b32_e32 v1, v1, v7, vcc
	v_sub_u32_e32 v7, v5, v6
	v_cndmask_b32_e32 v5, v5, v7, vcc
	v_cmp_ge_u32_e32 vcc, v5, v6
	v_add_u32_e32 v5, 1, v1
	s_nop 0
	v_cndmask_b32_e32 v1, v1, v5, vcc
	v_mad_u64_u32 v[6:7], s[4:5], v6, v1, v[6:7]
	v_cmp_ne_u32_e32 vcc, v3, v6
	s_and_saveexec_b64 s[4:5], vcc
	s_xor_b64 s[4:5], exec, s[4:5]
	s_cbranch_execz .LBB0_373
	v_mad_u32_u24 v255, v4, v1, 1
	v_mov_b32_e32 v3, s25
	v_add_co_u32_e32 v4, vcc, 0x2000, v3
	v_mov_b32_e32 v3, s24
	s_nop 0
	v_addc_co_u32_e32 v5, vcc, 0, v3, vcc
	flat_load_dword v3, v[4:5] offset:1024 sc1
	s_add_u32 s8, s25, 0x2400
	s_addc_u32 s9, s24, 0
	s_waitcnt vmcnt(0) lgkmcnt(0)
	v_cmp_lt_u32_e32 vcc, v3, v255
	s_and_saveexec_b64 s[6:7], vcc
	s_cbranch_execz .LBB0_372
	s_mov_b32 s26, 1
	s_mov_b64 s[10:11], 0
	s_branch .LBB0_364
